# attention tile loops: wave-uniform flag inversion done with one s_andn2_b64 instead of v_cndmask + v_cmp (12 sites where SCC is dead)
# speedup vs baseline: 1.0069x; 1.0069x over previous
.LBB0_713:
	s_nop 8
	v_cndmask_b32_e64 v196, v169, v97, s[0:1]
	v_cndmask_b32_e64 v97, v169, v96, s[0:1]
	v_cndmask_b32_e64 v96, v169, v95, s[0:1]
	v_cndmask_b32_e64 v95, v169, v94, s[0:1]
	v_cndmask_b32_e64 v94, v169, v93, s[0:1]
	v_cndmask_b32_e64 v93, v169, v92, s[0:1]
	v_cndmask_b32_e64 v92, v169, v91, s[0:1]
	v_cndmask_b32_e64 v91, v169, v90, s[0:1]
	v_cndmask_b32_e64 v90, v169, v89, s[0:1]
	v_cndmask_b32_e64 v89, v169, v88, s[0:1]
	v_cndmask_b32_e64 v88, v169, v87, s[0:1]
	v_cndmask_b32_e64 v87, v169, v86, s[0:1]
	v_cndmask_b32_e64 v86, v169, v85, s[0:1]
	v_cndmask_b32_e64 v85, v169, v84, s[0:1]
	v_cndmask_b32_e64 v84, v169, v83, s[0:1]
	v_cndmask_b32_e64 v83, v169, v82, s[0:1]
	s_andn2_b64 s[4:5], exec, s[30:31]
	s_andn2_b64 vcc, exec, s[30:31]
	s_mov_b64 s[8:9], -1
	s_cbranch_vccnz .LBB0_716
	v_mov_b32_e32 v82, 1.0
	s_cbranch_execz .LBB0_717
.LBB0_715:
	s_andn2_b64 s[8:9], exec, s[2:3]
	s_andn2_b64 vcc, exec, s[2:3]
	s_cbranch_vccz .LBB0_718
	s_branch .LBB0_720

.LBB0_717:
	v_max_f32_e32 v82, v84, v84
	v_max_f32_e32 v197, v83, v83
	v_max_f32_e32 v82, v197, v82
	v_max3_f32 v82, v82, v85, v86
	v_max3_f32 v82, v82, v87, v88
	v_max3_f32 v82, v82, v89, v90
	v_max3_f32 v82, v82, v91, v92
	v_max3_f32 v82, v82, v93, v94
	v_max3_f32 v82, v82, v95, v96
	v_max3_f32 v82, v82, v97, v196
	ds_bpermute_b32 v197, v171, v82
	s_waitcnt lgkmcnt(0)
	v_max3_f32 v197, v195, v82, v197
	v_sub_f32_e32 v82, v195, v197
	v_exp_f32_e32 v82, v82
	v_mov_b32_e32 v195, v197
	s_andn2_b64 s[8:9], exec, s[2:3]
	s_andn2_b64 vcc, exec, s[2:3]
	s_cbranch_vccnz .LBB0_720

.LBB0_740:
	s_nop 8
	v_cndmask_b32_e64 v196, v169, v97, s[0:1]
	v_cndmask_b32_e64 v97, v169, v96, s[0:1]
	v_cndmask_b32_e64 v96, v169, v95, s[0:1]
	v_cndmask_b32_e64 v95, v169, v94, s[0:1]
	v_cndmask_b32_e64 v94, v169, v93, s[0:1]
	v_cndmask_b32_e64 v93, v169, v92, s[0:1]
	v_cndmask_b32_e64 v92, v169, v91, s[0:1]
	v_cndmask_b32_e64 v91, v169, v90, s[0:1]
	v_cndmask_b32_e64 v90, v169, v89, s[0:1]
	v_cndmask_b32_e64 v89, v169, v88, s[0:1]
	v_cndmask_b32_e64 v88, v169, v87, s[0:1]
	v_cndmask_b32_e64 v87, v169, v86, s[0:1]
	v_cndmask_b32_e64 v86, v169, v85, s[0:1]
	v_cndmask_b32_e64 v85, v169, v84, s[0:1]
	v_cndmask_b32_e64 v84, v169, v83, s[0:1]
	v_cndmask_b32_e64 v83, v169, v82, s[0:1]
	s_andn2_b64 s[6:7], exec, s[30:31]
	s_andn2_b64 vcc, exec, s[30:31]
	s_mov_b64 s[8:9], -1
	s_cbranch_vccnz .LBB0_750
	v_mov_b32_e32 v82, 1.0
	s_cbranch_execz .LBB0_751

.LBB0_1787:
	s_andn2_b64 s[8:9], exec, s[28:29]
	s_andn2_b64 vcc, exec, s[28:29]
	s_cbranch_vccz .LBB0_1790
	s_branch .LBB0_1792

.LBB0_1789:
	v_max_f32_e32 v82, v84, v84
	v_max_f32_e32 v197, v83, v83
	v_max_f32_e32 v82, v197, v82
	v_max3_f32 v82, v82, v85, v86
	v_max3_f32 v82, v82, v87, v88
	v_max3_f32 v82, v82, v89, v90
	v_max3_f32 v82, v82, v91, v92
	v_max3_f32 v82, v82, v93, v94
	v_max3_f32 v82, v82, v95, v96
	v_max3_f32 v82, v82, v97, v196
	ds_bpermute_b32 v197, v171, v82
	s_waitcnt lgkmcnt(0)
	v_max3_f32 v197, v195, v82, v197
	v_sub_f32_e32 v82, v195, v197
	v_exp_f32_e32 v82, v82
	v_mov_b32_e32 v195, v197
	s_andn2_b64 s[8:9], exec, s[28:29]
	s_andn2_b64 vcc, exec, s[28:29]
	s_cbranch_vccnz .LBB0_1792
